# speedup vs baseline: 1.0226x; 1.0226x over previous
.LBB2_103:
	s_cmp_lg_u32 0, -1
	s_cselect_b32 s2, 0, 0
	s_addk_i32 s2, 0x6000
	v_add_u32_e32 v51, s2, v228
	v_add3_u32 v228, v51, v208, v230
	v_add_f32_e32 v51, v82, v83
	v_add_f32_e32 v51, v84, v51
	v_add_f32_e32 v51, v85, v51
	v_add_f32_e32 v51, v86, v51
	v_add_f32_e32 v51, v87, v51
	v_add_f32_e32 v51, v88, v51
	v_add_f32_e32 v51, v89, v51
	v_add_f32_e32 v51, v90, v51
	v_add_f32_e32 v51, v91, v51
	v_add_f32_e32 v51, v92, v51
	v_add_f32_e32 v51, v93, v51
	v_add_f32_e32 v51, v94, v51
	v_add_f32_e32 v51, v95, v51
	v_add_f32_e32 v51, v96, v51
	v_add_f32_e32 v51, v97, v51
	v_add_f32_e32 v51, v34, v51
	v_add_f32_e32 v51, v35, v51
	v_add_f32_e32 v51, v36, v51
	v_add_f32_e32 v51, v37, v51
	v_add_f32_e32 v51, v38, v51
	v_add_f32_e32 v51, v39, v51
	v_add_f32_e32 v51, v40, v51
	v_add_f32_e32 v51, v41, v51
	v_add_f32_e32 v51, v42, v51
	v_add_f32_e32 v51, v43, v51
	v_add_f32_e32 v51, v44, v51
	v_add_f32_e32 v51, v45, v51
	s_mov_b32 s2, m0
	s_mov_b32 m0, s35
	s_nop 0
	global_load_lds_dwordx4 v[212:213], off
	s_mov_b32 m0, s2
	v_add_f32_e32 v51, v46, v51
	s_mov_b32 s2, m0
	s_mov_b32 m0, s36
	s_nop 0
	global_load_lds_dwordx4 v[214:215], off
	s_mov_b32 m0, s2
	v_add_f32_e32 v51, v47, v51
	s_mov_b32 s2, m0
	s_mov_b32 m0, s37
	s_nop 0
	global_load_lds_dwordx4 v[216:217], off
	s_mov_b32 m0, s2
	v_add_f32_e32 v51, v48, v51
	v_add_f32_e32 v51, v49, v51
	v_add_f32_e32 v51, v114, v51
	v_cvt_pk_f16_f32 v34, v34, v35
	v_cvt_pk_f16_f32 v52, v82, v83
	v_cvt_pk_f16_f32 v53, v84, v85
	v_cvt_pk_f16_f32 v54, v86, v87
	v_cvt_pk_f16_f32 v55, v88, v89
	v_cvt_pk_f16_f32 v56, v90, v91
	v_cvt_pk_f16_f32 v57, v92, v93
	v_cvt_pk_f16_f32 v58, v94, v95
	v_cvt_pk_f16_f32 v59, v96, v97
	v_cvt_pk_f16_f32 v35, v36, v37
	v_cvt_pk_f16_f32 v36, v38, v39
	v_cvt_pk_f16_f32 v37, v40, v41
	v_cvt_pk_f16_f32 v38, v42, v43
	v_cvt_pk_f16_f32 v39, v44, v45
	v_cvt_pk_f16_f32 v40, v46, v47
	v_cvt_pk_f16_f32 v41, v48, v49
	v_add_u32_e32 v72, s40, v228
	ds_read_b64_tr_b16 v[42:43],v72 offset:0
	ds_read_b64_tr_b16 v[44:45],v72 offset:512
	ds_read_b64_tr_b16 v[46:47],v72 offset:1024
	ds_read_b64_tr_b16 v[48:49],v72 offset:1536
	ds_read_b64_tr_b16 v[60:61],v72 offset:2048
	ds_read_b64_tr_b16 v[62:63],v72 offset:2560
	ds_read_b64_tr_b16 v[64:65],v72 offset:3072
	ds_read_b64_tr_b16 v[66:67],v72 offset:3584
	s_waitcnt lgkmcnt(0)
	s_nop 0
	v_mfma_f32_32x32x16_f16 v[2:17], v[52:55], v[42:45], v[2:17]
	ds_read_b64_tr_b16 v[42:43],v72 offset:4096
	ds_read_b64_tr_b16 v[44:45],v72 offset:4608
	v_mfma_f32_32x32x16_f16 v[2:17], v[56:59], v[46:49], v[2:17]
	ds_read_b64_tr_b16 v[46:47],v72 offset:5120
	ds_read_b64_tr_b16 v[48:49],v72 offset:5632
	v_mfma_f32_32x32x16_f16 v[2:17], v[34:37], v[60:63], v[2:17]
	ds_read_b64_tr_b16 v[60:61],v72 offset:6144
	ds_read_b64_tr_b16 v[62:63],v72 offset:6656
	ds_read_b64_tr_b16 v[68:69],v72 offset:7168
	ds_read_b64_tr_b16 v[70:71],v72 offset:7680
	s_waitcnt lgkmcnt(0)
	v_mfma_f32_32x32x16_f16 v[2:17], v[38:41], v[64:67], v[2:17]
	v_mfma_f32_32x32x16_f16 v[18:33], v[52:55], v[42:45], v[18:33]
	v_mfma_f32_32x32x16_f16 v[18:33], v[56:59], v[46:49], v[18:33]
	v_mfma_f32_32x32x16_f16 v[18:33], v[34:37], v[60:63], v[18:33]
	v_mov_b32_e32 v34, v51
	s_nop 1
	v_permlane32_swap_b32_e32 v51, v34
	v_mfma_f32_32x32x16_f16 v[18:33], v[38:41], v[68:71], v[18:33]
	s_and_saveexec_b64 s[2:3], s[0:1]
	v_add_f32_e32 v34, v51, v34
	ds_write_b32 v223, v34 offset:49280
	s_or_b64 exec, exec, s[2:3]
	s_waitcnt lgkmcnt(0)
	ds_read_b128 v[34:37], v50 offset:49280
	ds_read_b128 v[38:41], v50 offset:49312
	s_lshl_b64 s[2:3], s[14:15], 1
	s_add_u32 s2, s10, s2
	s_addc_u32 s3, s11, s3
	s_waitcnt lgkmcnt(1)
	v_rcp_f32_e32 v42, v34
	v_rcp_f32_e32 v43, v35
	s_lshl_b32 s6, s34, 12
	s_add_i32 s6, s6, 0
	v_lshlrev_b32_e32 v230, 1, v222
	v_lshlrev_b32_e32 v231, 9, v211
	v_rcp_f32_e32 v44, v36
	v_rcp_f32_e32 v45, v37
	s_waitcnt lgkmcnt(0)
	v_rcp_f32_e32 v46, v38
	ds_read_b128 v[34:37], v50 offset:49344
	v_rcp_f32_e32 v47, v39
	v_rcp_f32_e32 v48, v40
	v_rcp_f32_e32 v49, v41
	ds_read_b128 v[38:41], v50 offset:49376
	v_add3_u32 v50, s6, v230, v231
	v_fma_mixlo_f16 v2, v2, v42, 0
	ds_write_b16 v50, v2 offset:51200
	v_fma_mixlo_f16 v2, v18, v42, 0
	ds_write_b16 v50, v2 offset:51264
	v_fma_mixlo_f16 v2, v3, v43, 0
	ds_write_b16 v50, v2 offset:51328
	v_fma_mixlo_f16 v2, v19, v43, 0
	ds_write_b16 v50, v2 offset:51392
	v_fma_mixlo_f16 v2, v4, v44, 0
	ds_write_b16 v50, v2 offset:51456
	v_fma_mixlo_f16 v2, v20, v44, 0
	ds_write_b16 v50, v2 offset:51520
	v_fma_mixlo_f16 v2, v5, v45, 0
	ds_write_b16 v50, v2 offset:51584
	v_fma_mixlo_f16 v2, v21, v45, 0
	ds_write_b16 v50, v2 offset:51648
	v_fma_mixlo_f16 v2, v6, v46, 0
	ds_write_b16 v50, v2 offset:52224
	v_fma_mixlo_f16 v2, v22, v46, 0
	ds_write_b16 v50, v2 offset:52288
	v_fma_mixlo_f16 v2, v7, v47, 0
	ds_write_b16 v50, v2 offset:52352
	v_fma_mixlo_f16 v2, v23, v47, 0
	s_waitcnt lgkmcnt(12)
	v_rcp_f32_e32 v34, v34
	ds_write_b16 v50, v2 offset:52416
	v_fma_mixlo_f16 v2, v8, v48, 0
	ds_write_b16 v50, v2 offset:52480
	v_fma_mixlo_f16 v2, v24, v48, 0
	v_rcp_f32_e32 v35, v35
	ds_write_b16 v50, v2 offset:52544
	v_fma_mixlo_f16 v2, v9, v49, 0
	ds_write_b16 v50, v2 offset:52608
	v_fma_mixlo_f16 v2, v25, v49, 0
	v_rcp_f32_e32 v36, v36
	ds_write_b16 v50, v2 offset:52672
	v_fma_mixlo_f16 v2, v10, v34, 0
	ds_write_b16 v50, v2 offset:53248
	v_fma_mixlo_f16 v2, v26, v34, 0
	v_rcp_f32_e32 v37, v37
	ds_write_b16 v50, v2 offset:53312
	v_fma_mixlo_f16 v2, v11, v35, 0
	ds_write_b16 v50, v2 offset:53376
	v_fma_mixlo_f16 v2, v27, v35, 0
	s_waitcnt lgkmcnt(14)
	v_rcp_f32_e32 v38, v38
	ds_write_b16 v50, v2 offset:53440
	v_fma_mixlo_f16 v2, v12, v36, 0
	ds_write_b16 v50, v2 offset:53504
	v_fma_mixlo_f16 v2, v28, v36, 0
	v_rcp_f32_e32 v39, v39
	ds_write_b16 v50, v2 offset:53568
	v_fma_mixlo_f16 v2, v13, v37, 0
	ds_write_b16 v50, v2 offset:53632
	v_fma_mixlo_f16 v2, v29, v37, 0
	v_rcp_f32_e32 v40, v40
	ds_write_b16 v50, v2 offset:53696
	v_fma_mixlo_f16 v2, v14, v38, 0
	ds_write_b16 v50, v2 offset:54272
	v_fma_mixlo_f16 v2, v30, v38, 0
	v_rcp_f32_e32 v41, v41
	ds_write_b16 v50, v2 offset:54336
	v_fma_mixlo_f16 v2, v15, v39, 0
	ds_write_b16 v50, v2 offset:54400
	v_fma_mixlo_f16 v2, v31, v39, 0
	ds_write_b16 v50, v2 offset:54464
	v_fma_mixlo_f16 v2, v16, v40, 0
	ds_write_b16 v50, v2 offset:54528
	v_fma_mixlo_f16 v2, v32, v40, 0
	ds_write_b16 v50, v2 offset:54592
	v_fma_mixlo_f16 v2, v17, v41, 0
	ds_write_b16 v50, v2 offset:54656
	v_fma_mixlo_f16 v2, v33, v41, 0
	ds_write_b16 v50, v2 offset:54720
	v_and_b32_e32 v2, 56, v209
	s_lshl_b32 s22, s33, 1
	v_lshrrev_b32_e32 v36, 3, v207
	v_lshlrev_b32_e32 v220, 1, v2
	s_add_u32 s2, s2, s22
	v_add_u32_e32 v14, s6, v220
	v_lshlrev_b32_e32 v232, 7, v36
	s_addc_u32 s3, s3, 0
	s_waitcnt lgkmcnt(0)
	v_mov_b32_e32 v221, 0
	v_add_u32_e32 v2, v14, v232
	v_or_b32_e32 v37, 8, v36
	v_lshl_add_u64 v[10:11], s[2:3], 0, v[220:221]
	ds_read_b128 v[2:5], v2 offset:51200
	v_lshlrev_b32_e32 v6, 11, v36
	v_mov_b32_e32 v7, v221
	v_lshlrev_b32_e32 v233, 7, v37
	v_readfirstlane_b32 s8, v0
	v_lshl_add_u64 v[12:13], v[10:11], 0, v[6:7]
	v_add_u32_e32 v6, v14, v233
	s_lshr_b32 s23, s8, 6
	ds_read_b128 v[6:9], v6 offset:51200
	s_or_b32 s2, s12, s27
	s_lshl_b32 s12, s23, 5
	s_add_u32 s6, s2, s12
	s_addc_u32 s7, s13, 0
	s_waitcnt lgkmcnt(1)
	global_store_dwordx4 v[12:13], v[2:5], off sc1
	v_or_b32_e32 v38, 16, v36
	s_lshl_b64 s[2:3], s[6:7], 11
	v_lshlrev_b32_e32 v2, 11, v37
	v_mov_b32_e32 v3, v221
	v_lshl_add_u64 v[2:3], v[10:11], 0, v[2:3]
	v_lshlrev_b32_e32 v234, 7, v38
	s_add_u32 s2, s4, s2
	s_waitcnt lgkmcnt(0)
	global_store_dwordx4 v[2:3], v[6:9], off sc1
	v_add_u32_e32 v2, v14, v234
	v_or_b32_e32 v39, 24, v36
	s_addc_u32 s3, s5, s3
	ds_read_b128 v[2:5], v2 offset:51200
	v_lshlrev_b32_e32 v6, 11, v38
	v_mov_b32_e32 v7, v221
	v_lshlrev_b32_e32 v235, 7, v39
	s_add_u32 s2, s2, s22
	v_lshl_add_u64 v[12:13], v[10:11], 0, v[6:7]
	v_add_u32_e32 v6, v14, v235
	s_addc_u32 s3, s3, 0
	s_lshl_b32 s4, s8, 4
	ds_read_b128 v[6:9], v6 offset:51200
	s_and_b32 s4, s4, 0xfffff000
	s_add_u32 s4, s30, s4
	s_addc_u32 s5, s31, 0
	s_lshr_b32 s9, s8, 2
	s_waitcnt lgkmcnt(1)
	global_store_dwordx4 v[12:13], v[2:5], off sc1
	v_and_or_b32 v0, s9, 48, v1
	s_lshl_b32 s9, s23, 10
	v_lshlrev_b32_e32 v2, 11, v39
	v_mov_b32_e32 v3, v221
	v_lshl_add_u64 v[2:3], v[10:11], 0, v[2:3]
	v_lshlrev_b32_e32 v0, 6, v0
	v_mov_b32_e32 v1, v221
	s_cmp_lg_u32 0, -1
	s_waitcnt lgkmcnt(0)
	global_store_dwordx4 v[2:3], v[6:9], off sc1
	v_lshl_add_u64 v[0:1], s[4:5], 0, v[0:1]
	s_cselect_b32 s4, 0, 0
	s_waitcnt lgkmcnt(0)
	s_barrier
	v_lshlrev_b32_e32 v2, 1, v208
	v_mov_b32_e32 v3, v221
	s_add_i32 s25, s4, s9
	v_lshl_add_u64 v[208:209], v[0:1], 0, v[2:3]
	s_addk_i32 s25, 0x6000
	s_mov_b32 s4, m0
	s_mov_b32 m0, s25
	s_nop 0
	global_load_lds_dwordx4 v[208:209], off
	s_mov_b32 m0, s4
	v_lshlrev_b32_e32 v0, 1, v210
	global_load_dwordx4 v[156:159], v0, s[2:3]
	global_load_dwordx4 v[152:155], v0, s[2:3] offset:32
	global_load_dwordx4 v[148:151], v0, s[2:3] offset:64
	global_load_dwordx4 v[144:147], v0, s[2:3] offset:96
	v_mov_b32_e32 v0, v221
	v_mov_b32_e32 v1, v221
	v_mov_b32_e32 v2, v221
	v_mov_b32_e32 v4, v221
	v_mov_b32_e32 v5, v221
	v_mov_b32_e32 v6, v221
	v_mov_b32_e32 v7, v221
	v_mov_b32_e32 v8, v221
	v_mov_b32_e32 v9, v221
	v_mov_b32_e32 v10, v221
	v_mov_b32_e32 v11, v221
	v_mov_b32_e32 v12, v221
	v_mov_b32_e32 v13, v221
	v_mov_b32_e32 v14, v221
	v_mov_b32_e32 v15, v221
	s_waitcnt vmcnt(5) lgkmcnt(0)
	s_barrier
	ds_read_b128 v[32:35], v224
	s_cmp_lg_u32 s26, 0
	s_waitcnt vmcnt(3) lgkmcnt(0)
	v_mfma_f32_32x32x16_f16 v[16:31], v[32:35], v[156:159], v[0:15]
	ds_read_b128 v[32:35], v224 offset:512
	s_cselect_b64 s[2:3], -1, 0
	v_lshlrev_b32_e32 v239, 10, v36
	v_lshlrev_b32_e32 v238, 10, v37
	v_lshlrev_b32_e32 v237, 10, v38
	v_lshlrev_b32_e32 v236, 10, v39
	v_or_b32_e32 v221, s12, v222
	s_waitcnt lgkmcnt(0)
	v_mfma_f32_32x32x16_f16 v[0:15], v[32:35], v[156:159], v[0:15]
	ds_read_b128 v[32:35], v224 offset:2048
	s_and_b64 vcc, exec, s[2:3]
	s_waitcnt vmcnt(2) lgkmcnt(0)
	v_mfma_f32_32x32x16_f16 v[16:31], v[32:35], v[152:155], v[16:31]
	ds_read_b128 v[32:35], v224 offset:2560
	s_waitcnt lgkmcnt(0)
	v_mfma_f32_32x32x16_f16 v[0:15], v[32:35], v[152:155], v[0:15]
	ds_read_b128 v[32:35], v224 offset:4096
	s_waitcnt vmcnt(1) lgkmcnt(0)
	v_mfma_f32_32x32x16_f16 v[16:31], v[32:35], v[148:151], v[16:31]
	ds_read_b128 v[32:35], v224 offset:4608
	s_waitcnt lgkmcnt(0)
	v_mfma_f32_32x32x16_f16 v[0:15], v[32:35], v[148:151], v[0:15]
	ds_read_b128 v[32:35], v224 offset:6144
	s_waitcnt vmcnt(0) lgkmcnt(0)
	v_mfma_f32_32x32x16_f16 v[16:31], v[32:35], v[144:147], v[16:31]
	ds_read_b128 v[32:35], v224 offset:6656
	s_waitcnt lgkmcnt(0)
	v_mfma_f32_32x32x16_f16 v[0:15], v[32:35], v[144:147], v[0:15]
	s_nop 15
	s_nop 7
	s_cbranch_vccnz .LBB2_119
	v_readfirstlane_b32 s12, v221
	s_cmp_lt_i32 s12, 0
	s_cbranch_scc1 .LBB2_111
	s_cmp_gt_u32 s12, 31
	s_cbranch_scc1 .LBB2_112
	v_mov_b32_e32 v32, 0xff800000
	v_cmp_lt_u32_e32 vcc, v227, v221
	v_or_b32_e32 v33, 2, v227
	s_mov_b32 s13, 0xff800000
	v_cndmask_b32_e32 v17, v32, v17, vcc
	v_cmp_le_u32_e32 vcc, v227, v221
	s_nop 1
	v_cndmask_b32_e32 v16, v32, v16, vcc
	v_cmp_le_u32_e32 vcc, v33, v221
	v_or_b32_e32 v33, 3, v227
	s_nop 0
	v_cndmask_b32_e32 v18, v32, v18, vcc
	v_cmp_le_u32_e32 vcc, v33, v221
	v_or_b32_e32 v33, 8, v227
	s_nop 0
	v_cndmask_b32_e32 v19, v32, v19, vcc
	v_cmp_le_u32_e32 vcc, v33, v221
	v_or_b32_e32 v33, 9, v227
	s_nop 0
	v_cndmask_b32_e32 v20, v32, v20, vcc
	v_cmp_le_u32_e32 vcc, v33, v221
	v_or_b32_e32 v33, 10, v227
	s_nop 0
	v_cndmask_b32_e32 v21, v32, v21, vcc
	v_cmp_le_u32_e32 vcc, v33, v221
	v_or_b32_e32 v33, 11, v227
	s_nop 0
	v_cndmask_b32_e32 v22, v32, v22, vcc
	v_cmp_le_u32_e32 vcc, v33, v221
	v_or_b32_e32 v33, 16, v227
	s_nop 0
	v_cndmask_b32_e32 v23, v32, v23, vcc
	v_cmp_le_u32_e32 vcc, v33, v221
	v_or_b32_e32 v33, 17, v227
	s_nop 0
	v_cndmask_b32_e32 v24, v32, v24, vcc
	v_cmp_le_u32_e32 vcc, v33, v221
	v_or_b32_e32 v33, 18, v227
	s_nop 0
	v_cndmask_b32_e32 v25, v32, v25, vcc
	v_cmp_le_u32_e32 vcc, v33, v221
	v_or_b32_e32 v33, 19, v227
	s_nop 0
	v_cndmask_b32_e32 v26, v32, v26, vcc
	v_cmp_le_u32_e32 vcc, v33, v221
	v_or_b32_e32 v33, 24, v227
	s_nop 0
	v_cndmask_b32_e32 v27, v32, v27, vcc
	v_cmp_le_u32_e32 vcc, v33, v221
	v_or_b32_e32 v33, 25, v227
	s_nop 0
	v_cndmask_b32_e32 v28, v32, v28, vcc
	v_cmp_le_u32_e32 vcc, v33, v221
	v_or_b32_e32 v33, 26, v227
	s_nop 0
	v_cndmask_b32_e32 v29, v32, v29, vcc
	v_cmp_le_u32_e32 vcc, v33, v221
	s_nop 1
	v_cndmask_b32_e32 v30, v32, v30, vcc
	v_or_b32_e32 v32, 27, v227
	v_cmp_gt_u32_e32 vcc, v32, v221
	s_and_saveexec_b64 s[4:5], vcc
	v_mov_b32_e32 v31, s13
	s_or_b64 exec, exec, s[4:5]
	s_branch .LBB2_112

.LBB2_224:
	v_add_f32_e32 v49, v96, v97
	v_add_f32_e32 v49, v98, v49
	v_add_f32_e32 v49, v99, v49
	v_add_f32_e32 v49, v100, v49
	v_add_f32_e32 v49, v101, v49
	v_add_f32_e32 v49, v102, v49
	v_add_f32_e32 v49, v103, v49
	v_add_f32_e32 v49, v104, v49
	v_add_f32_e32 v49, v105, v49
	v_add_f32_e32 v49, v106, v49
	v_add_f32_e32 v49, v107, v49
	v_add_f32_e32 v49, v108, v49
	v_add_f32_e32 v49, v109, v49
	v_add_f32_e32 v49, v110, v49
	v_add_f32_e32 v49, v111, v49
	v_add_f32_e32 v49, v32, v49
	v_add_f32_e32 v49, v33, v49
	v_add_f32_e32 v49, v34, v49
	v_add_f32_e32 v49, v35, v49
	v_add_f32_e32 v49, v36, v49
	v_add_f32_e32 v49, v37, v49
	v_add_f32_e32 v49, v38, v49
	v_add_f32_e32 v49, v39, v49
	v_add_f32_e32 v49, v40, v49
	v_add_f32_e32 v49, v41, v49
	v_add_f32_e32 v49, v42, v49
	v_add_f32_e32 v49, v43, v49
	v_add_f32_e32 v49, v44, v49
	v_add_f32_e32 v49, v45, v49
	v_add_f32_e32 v49, v46, v49
	v_add_f32_e32 v49, v47, v49
	v_add_f32_e32 v49, v72, v49
	v_cvt_pk_f16_f32 v32, v32, v33
	v_cvt_pk_f16_f32 v50, v96, v97
	v_cvt_pk_f16_f32 v51, v98, v99
	v_cvt_pk_f16_f32 v52, v100, v101
	v_cvt_pk_f16_f32 v53, v102, v103
	v_cvt_pk_f16_f32 v54, v104, v105
	v_cvt_pk_f16_f32 v55, v106, v107
	v_cvt_pk_f16_f32 v56, v108, v109
	v_cvt_pk_f16_f32 v57, v110, v111
	v_cvt_pk_f16_f32 v33, v34, v35
	v_cvt_pk_f16_f32 v34, v36, v37
	v_cvt_pk_f16_f32 v35, v38, v39
	v_cvt_pk_f16_f32 v36, v40, v41
	v_cvt_pk_f16_f32 v37, v42, v43
	v_cvt_pk_f16_f32 v38, v44, v45
	v_cvt_pk_f16_f32 v39, v46, v47
	v_add_u32_e32 v70, s30, v228
	ds_read_b64_tr_b16 v[40:41],v70 offset:0
	ds_read_b64_tr_b16 v[42:43],v70 offset:512
	ds_read_b64_tr_b16 v[44:45],v70 offset:1024
	ds_read_b64_tr_b16 v[46:47],v70 offset:1536
	ds_read_b64_tr_b16 v[58:59],v70 offset:2048
	ds_read_b64_tr_b16 v[60:61],v70 offset:2560
	ds_read_b64_tr_b16 v[62:63],v70 offset:3072
	ds_read_b64_tr_b16 v[64:65],v70 offset:3584
	s_waitcnt lgkmcnt(0)
	s_nop 0
	v_mfma_f32_32x32x16_f16 v[0:15], v[50:53], v[40:43], v[0:15]
	ds_read_b64_tr_b16 v[40:41],v70 offset:4096
	ds_read_b64_tr_b16 v[42:43],v70 offset:4608
	v_mfma_f32_32x32x16_f16 v[0:15], v[54:57], v[44:47], v[0:15]
	ds_read_b64_tr_b16 v[44:45],v70 offset:5120
	ds_read_b64_tr_b16 v[46:47],v70 offset:5632
	v_mfma_f32_32x32x16_f16 v[0:15], v[32:35], v[58:61], v[0:15]
	ds_read_b64_tr_b16 v[58:59],v70 offset:6144
	ds_read_b64_tr_b16 v[60:61],v70 offset:6656
	ds_read_b64_tr_b16 v[66:67],v70 offset:7168
	ds_read_b64_tr_b16 v[68:69],v70 offset:7680
	s_waitcnt lgkmcnt(0)
	v_mfma_f32_32x32x16_f16 v[0:15], v[36:39], v[62:65], v[0:15]
	v_mfma_f32_32x32x16_f16 v[16:31], v[50:53], v[40:43], v[16:31]
	v_mfma_f32_32x32x16_f16 v[16:31], v[54:57], v[44:47], v[16:31]
	v_mfma_f32_32x32x16_f16 v[16:31], v[32:35], v[58:61], v[16:31]
	v_mov_b32_e32 v32, v49
	s_nop 1
	v_permlane32_swap_b32_e32 v49, v32
	v_mfma_f32_32x32x16_f16 v[16:31], v[36:39], v[66:69], v[16:31]
	s_and_saveexec_b64 s[2:3], s[0:1]
	v_add_f32_e32 v32, v49, v32
	ds_write_b32 v240, v32 offset:49280
	s_or_b64 exec, exec, s[2:3]
	s_waitcnt lgkmcnt(0)
	ds_read_b128 v[32:35], v48 offset:49280
	ds_read_b128 v[36:39], v48 offset:49312
	s_lshl_b64 s[0:1], s[4:5], 1
	s_add_u32 s0, s10, s0
	s_addc_u32 s1, s11, s1
	s_waitcnt lgkmcnt(1)
	v_rcp_f32_e32 v40, v32
	v_rcp_f32_e32 v41, v33
	s_lshl_b32 s2, s23, 12
	s_add_i32 s2, s2, 0
	v_rcp_f32_e32 v42, v34
	v_rcp_f32_e32 v43, v35
	s_waitcnt lgkmcnt(0)
	v_rcp_f32_e32 v44, v36
	ds_read_b128 v[32:35], v48 offset:49344
	v_rcp_f32_e32 v45, v37
	v_rcp_f32_e32 v46, v38
	v_rcp_f32_e32 v47, v39
	ds_read_b128 v[36:39], v48 offset:49376
	v_add3_u32 v48, s2, v230, v231
	v_fma_mixlo_f16 v0, v0, v40, 0
	ds_write_b16 v48, v0 offset:51200
	v_fma_mixlo_f16 v0, v16, v40, 0
	ds_write_b16 v48, v0 offset:51264
	v_fma_mixlo_f16 v0, v1, v41, 0
	ds_write_b16 v48, v0 offset:51328
	v_fma_mixlo_f16 v0, v17, v41, 0
	ds_write_b16 v48, v0 offset:51392
	v_fma_mixlo_f16 v0, v2, v42, 0
	ds_write_b16 v48, v0 offset:51456
	v_fma_mixlo_f16 v0, v18, v42, 0
	ds_write_b16 v48, v0 offset:51520
	v_fma_mixlo_f16 v0, v3, v43, 0
	ds_write_b16 v48, v0 offset:51584
	v_fma_mixlo_f16 v0, v19, v43, 0
	ds_write_b16 v48, v0 offset:51648
	v_fma_mixlo_f16 v0, v4, v44, 0
	ds_write_b16 v48, v0 offset:52224
	v_fma_mixlo_f16 v0, v20, v44, 0
	ds_write_b16 v48, v0 offset:52288
	v_fma_mixlo_f16 v0, v5, v45, 0
	ds_write_b16 v48, v0 offset:52352
	v_fma_mixlo_f16 v0, v21, v45, 0
	s_waitcnt lgkmcnt(12)
	v_rcp_f32_e32 v32, v32
	ds_write_b16 v48, v0 offset:52416
	v_fma_mixlo_f16 v0, v6, v46, 0
	ds_write_b16 v48, v0 offset:52480
	v_fma_mixlo_f16 v0, v22, v46, 0
	v_rcp_f32_e32 v33, v33
	ds_write_b16 v48, v0 offset:52544
	v_fma_mixlo_f16 v0, v7, v47, 0
	ds_write_b16 v48, v0 offset:52608
	v_fma_mixlo_f16 v0, v23, v47, 0
	v_rcp_f32_e32 v34, v34
	ds_write_b16 v48, v0 offset:52672
	v_fma_mixlo_f16 v0, v8, v32, 0
	ds_write_b16 v48, v0 offset:53248
	v_fma_mixlo_f16 v0, v24, v32, 0
	v_rcp_f32_e32 v35, v35
	ds_write_b16 v48, v0 offset:53312
	v_fma_mixlo_f16 v0, v9, v33, 0
	ds_write_b16 v48, v0 offset:53376
	v_fma_mixlo_f16 v0, v25, v33, 0
	s_waitcnt lgkmcnt(14)
	v_rcp_f32_e32 v36, v36
	ds_write_b16 v48, v0 offset:53440
	v_fma_mixlo_f16 v0, v10, v34, 0
	ds_write_b16 v48, v0 offset:53504
	v_fma_mixlo_f16 v0, v26, v34, 0
	v_rcp_f32_e32 v37, v37
	ds_write_b16 v48, v0 offset:53568
	v_fma_mixlo_f16 v0, v11, v35, 0
	ds_write_b16 v48, v0 offset:53632
	v_fma_mixlo_f16 v0, v27, v35, 0
	v_rcp_f32_e32 v38, v38
	ds_write_b16 v48, v0 offset:53696
	v_fma_mixlo_f16 v0, v12, v36, 0
	ds_write_b16 v48, v0 offset:54272
	v_fma_mixlo_f16 v0, v28, v36, 0
	v_rcp_f32_e32 v39, v39
	ds_write_b16 v48, v0 offset:54336
	v_fma_mixlo_f16 v0, v13, v37, 0
	ds_write_b16 v48, v0 offset:54400
	v_fma_mixlo_f16 v0, v29, v37, 0
	ds_write_b16 v48, v0 offset:54464
	v_fma_mixlo_f16 v0, v14, v38, 0
	ds_write_b16 v48, v0 offset:54528
	v_fma_mixlo_f16 v0, v30, v38, 0
	ds_write_b16 v48, v0 offset:54592
	v_fma_mixlo_f16 v0, v15, v39, 0
	ds_write_b16 v48, v0 offset:54656
	v_fma_mixlo_f16 v0, v31, v39, 0
	ds_write_b16 v48, v0 offset:54720
	v_add_u32_e32 v12, s2, v220
	s_waitcnt lgkmcnt(0)
	v_add_u32_e32 v0, v12, v232
	ds_read_b128 v[0:3], v0 offset:51200
	v_add_u32_e32 v4, v12, v233
	s_add_u32 s0, s0, s22
	ds_read_b128 v[4:7], v4 offset:51200
	s_addc_u32 s1, s1, 0
	v_mov_b32_e32 v221, 0
	v_lshl_add_u64 v[8:9], s[0:1], 0, v[220:221]
	v_lshlrev_b32_e32 v220, 1, v239
	v_lshl_add_u64 v[10:11], v[8:9], 0, v[220:221]
	v_lshlrev_b32_e32 v220, 1, v238
	s_waitcnt lgkmcnt(1)
	global_store_dwordx4 v[10:11], v[0:3], off sc1
	s_nop 1
	v_lshl_add_u64 v[0:1], v[8:9], 0, v[220:221]
	s_waitcnt lgkmcnt(0)
	global_store_dwordx4 v[0:1], v[4:7], off sc1
	v_add_u32_e32 v0, v12, v234
	ds_read_b128 v[0:3], v0 offset:51200
	v_add_u32_e32 v4, v12, v235
	ds_read_b128 v[4:7], v4 offset:51200
	v_lshlrev_b32_e32 v220, 1, v237
	v_lshl_add_u64 v[10:11], v[8:9], 0, v[220:221]
	v_lshlrev_b32_e32 v220, 1, v236
	s_waitcnt lgkmcnt(1)
	global_store_dwordx4 v[10:11], v[0:3], off sc1
	s_nop 1
	v_lshl_add_u64 v[0:1], v[8:9], 0, v[220:221]
	s_waitcnt lgkmcnt(0)
	global_store_dwordx4 v[0:1], v[4:7], off sc1
	s_waitcnt lgkmcnt(0)
	s_barrier
	s_endpgm

.LBB3_11:
	v_lshl_or_b32 v64, s46, 8, v134
	v_lshl_add_u32 v68, s45, 7, v132
	v_ashrrev_i32_e32 v65, 31, v64
	s_waitcnt lgkmcnt(0)
	v_mad_i64_i32 v[66:67], s[22:23], v68, s44, 0
	v_lshl_add_u64 v[66:67], v[66:67], 2, s[14:15]
	v_lshlrev_b64 v[64:65], 2, v[64:65]
	v_lshl_add_u64 v[66:67], v[66:67], 0, v[64:65]
	global_store_dwordx4 v[66:67], v[60:63], off sc1
	global_store_dwordx4 v[66:67], v[56:59], off offset:64 sc1
	global_store_dwordx4 v[66:67], v[52:55], off offset:512 sc1
	global_store_dwordx4 v[66:67], v[48:51], off offset:576 sc1
	s_cmp_eq_u32 s4, s43
	s_mov_b64 s[24:25], s[20:21]
	v_or_b32_e32 v48, 16, v68
	v_mad_i64_i32 v[48:49], s[22:23], v48, s44, 0
	v_lshl_add_u64 v[48:49], v[48:49], 2, s[14:15]
	v_lshl_add_u64 v[48:49], v[48:49], 0, v[64:65]
	global_store_dwordx4 v[48:49], v[44:47], off sc1
	global_store_dwordx4 v[48:49], v[40:43], off offset:64 sc1
	global_store_dwordx4 v[48:49], v[36:39], off offset:512 sc1
	global_store_dwordx4 v[48:49], v[32:35], off offset:576 sc1
	s_mov_b32 s45, s50
	s_mov_b32 s46, s49
	v_or_b32_e32 v32, 32, v68
	v_mad_i64_i32 v[32:33], s[22:23], v32, s44, 0
	v_lshl_add_u64 v[32:33], v[32:33], 2, s[14:15]
	v_lshl_add_u64 v[32:33], v[32:33], 0, v[64:65]
	global_store_dwordx4 v[32:33], v[28:31], off sc1
	global_store_dwordx4 v[32:33], v[24:27], off offset:64 sc1
	global_store_dwordx4 v[32:33], v[20:23], off offset:512 sc1
	global_store_dwordx4 v[32:33], v[16:19], off offset:576 sc1
	s_nop 1
	v_or_b32_e32 v16, 48, v68
	v_mad_i64_i32 v[16:17], s[22:23], v16, s44, 0
	v_lshl_add_u64 v[16:17], v[16:17], 2, s[14:15]
	v_lshl_add_u64 v[16:17], v[16:17], 0, v[64:65]
	s_mov_b64 s[22:23], s[18:19]
	global_store_dwordx4 v[16:17], v[12:15], off sc1
	global_store_dwordx4 v[16:17], v[8:11], off offset:64 sc1
	global_store_dwordx4 v[16:17], v[4:7], off offset:512 sc1
	global_store_dwordx4 v[16:17], v[0:3], off offset:576 sc1
	s_cbranch_scc1 .LBB3_27

	.text
	.p2alignl 6, 3212836864
	.fill 256, 4, 3212836864
	.p2alignl 8, 3212836864
